# combined: gelu packed epilogue + WATT A-set wait vmcnt(2) + FIN waits behind stores + DATT tail e4m3->bf16 direct conversion
# speedup vs baseline: 1.0125x; 1.0072x over previous
; __device__ __forceinline__ unsigned cvt_pk_bf16(float lo, float hi) { unsigned r; asm volatile("v_cvt_pk_bf16_f32 %0, %1, %2" : "=v"(r) : "v"(lo), "v"(hi)); return r; }
; #define DS_LOADQ(pa) do { const unsigned _q = roff(64 * (c.a0 + (pa)) + 32 * par + r32) + (unsigned)hi * 8u; _Pragma("unroll") for (int d0 = 0; d0 < 8; ++d0) qraw[d0] = *(const u32x2*)(zb + (_q + d0 * 16u)); } while (0)
; #define DS_RESET() do { m_reg = -1e30f; l_reg = 0.f; _Pragma("unroll") for (int d = 0; d < 4; ++d) _Pragma("unroll") for (int r = 0; r < 16; ++r) o[d][r] = 0.f; } while (0)
; __device__ __forceinline__ bf16x8 f8tob(u32x2 v) {
;     typedef float f2_ __attribute__((ext_vector_type(2)));
;     const f2_ a = __builtin_amdgcn_cvt_pk_f32_fp8((int)v.x, false), b = __builtin_amdgcn_cvt_pk_f32_fp8((int)v.x, true), c = __builtin_amdgcn_cvt_pk_f32_fp8((int)v.y, false), d = __builtin_amdgcn_cvt_pk_f32_fp8((int)v.y, true);
;     u32x4 w; w.x = cvt_pk_bf16(a[0], a[1]); w.y = cvt_pk_bf16(b[0], b[1]); w.z = cvt_pk_bf16(c[0], c[1]); w.w = cvt_pk_bf16(d[0], d[1]);
;     return __builtin_bit_cast(bf16x8, w);
; }
; __device__ __forceinline__ void datt_stream(LAS unsigned char* lds, const DattRun& c, const float C, const int wv) {
;     ...
;     bf16x8 qr[8]; u32x2 qraw[8]; float m_reg = -1e30f, l_reg = 0.f; f32x16 o[4];
;     ...
;     DS_LOADQ(pa0); DS_RESET();
;     auto compute = [&](const int rel, const int b, const int pa) __attribute__((always_inline)) {
;         const int tr = edge ? 0 : (rel == 1 ? 1 : (par ? (rel == 0 ? 2 : 0) : (rel == 2 ? 3 : 0))); const bool do0 = tr != 2, do1 = tr != 3;
;         if (rel == 0) {
; #pragma unroll
;             for (int d0 = 0; d0 < 8; ++d0) qr[d0] = f8tob(qraw[d0]); }
.LBB0_467:
	s_waitcnt vmcnt(4)
	v_cvt_scalef32_pk_bf16_fp8 v0, v206, 1.0
	v_cvt_scalef32_pk_bf16_fp8 v1, v206, 1.0 op_sel:[1,0,0]
	v_cvt_scalef32_pk_bf16_fp8 v2, v207, 1.0
	v_cvt_scalef32_pk_bf16_fp8 v3, v207, 1.0 op_sel:[1,0,0]
	ds_write_b128 v225, v[0:3] offset:16384
	s_waitcnt vmcnt(4)
	v_cvt_scalef32_pk_bf16_fp8 v0, v202, 1.0
	v_cvt_scalef32_pk_bf16_fp8 v1, v202, 1.0 op_sel:[1,0,0]
	v_cvt_scalef32_pk_bf16_fp8 v2, v203, 1.0
	v_cvt_scalef32_pk_bf16_fp8 v3, v203, 1.0 op_sel:[1,0,0]
	ds_write_b128 v226, v[0:3] offset:49152
	s_waitcnt vmcnt(4)
	v_cvt_scalef32_pk_bf16_fp8 v0, v198, 1.0
	v_cvt_scalef32_pk_bf16_fp8 v1, v198, 1.0 op_sel:[1,0,0]
	v_cvt_scalef32_pk_bf16_fp8 v2, v199, 1.0
	v_cvt_scalef32_pk_bf16_fp8 v3, v199, 1.0 op_sel:[1,0,0]
	s_add_i32 s0, s57, 3
	ds_write_b128 v227, v[0:3] offset:16384
	s_waitcnt vmcnt(4)
	s_min_i32 s0, s0, s81
	v_cvt_scalef32_pk_bf16_fp8 v0, v194, 1.0
	v_cvt_scalef32_pk_bf16_fp8 v1, v194, 1.0 op_sel:[1,0,0]
	v_cvt_scalef32_pk_bf16_fp8 v2, v195, 1.0
	v_add_u32_e32 v4, s0, v224
	v_cvt_scalef32_pk_bf16_fp8 v3, v195, 1.0 op_sel:[1,0,0]
	v_lshl_add_u32 v6, v4, 6, v197
	v_add_u32_e32 v4, 32, v6
	v_min_i32_e32 v4, s95, v4
	v_cmp_lt_i32_e32 vcc, s43, v6
	v_min_i32_e32 v7, s95, v6
	s_cmp_gt_u32 s57, s61
	v_cndmask_b32_e32 v4, 0, v4, vcc
	v_cmp_lt_i32_e32 vcc, -1, v6
	v_lshlrev_b32_e32 v4, s45, v4
	v_add_u32_e32 v4, s56, v4
	v_cndmask_b32_e32 v6, 0, v7, vcc
	v_lshlrev_b32_e32 v6, s45, v6
	v_mad_u64_u32 v[4:5], s[0:1], v4, s42, v[196:197]
	v_add_u32_e32 v6, s56, v6
	v_add_u32_e32 v5, 0x400, v4
	v_mad_u64_u32 v[6:7], s[0:1], v6, s42, v[196:197]
	v_add_u32_e32 v7, 0x400, v6
	global_load_dwordx2 v[198:199], v5, s[92:93]
	global_load_dwordx2 v[206:207], v7, s[92:93]
	global_load_dwordx2 v[202:203], v6, s[92:93]
	global_load_dwordx2 v[194:195], v4, s[92:93]
	s_cselect_b64 s[0:1], -1, 0
	s_and_b64 vcc, exec, s[0:1]
	ds_write_b128 v228, v[0:3] offset:49152
	s_cmp_eq_u32 s101, 2
	s_cbranch_scc0 .Ldatt_qc0_skip
	v_cvt_pk_f32_fp8_e32 v[0:1], v176
	v_cvt_pk_f32_fp8_sdwa v[2:3], v176 src0_sel:WORD_1
	v_cvt_pk_f32_fp8_e32 v[4:5], v177
	v_cvt_pk_f32_fp8_sdwa v[6:7], v177 src0_sel:WORD_1
	v_cvt_pk_bf16_f32 v144, v0, v1
	v_cvt_pk_bf16_f32 v145, v2, v3
	v_cvt_pk_bf16_f32 v146, v4, v5
	v_cvt_pk_bf16_f32 v147, v6, v7
	v_cvt_pk_f32_fp8_e32 v[0:1], v178
	v_cvt_pk_f32_fp8_sdwa v[2:3], v178 src0_sel:WORD_1
	v_cvt_pk_f32_fp8_e32 v[4:5], v179
	v_cvt_pk_f32_fp8_sdwa v[6:7], v179 src0_sel:WORD_1
	v_cvt_pk_bf16_f32 v148, v0, v1
	v_cvt_pk_bf16_f32 v149, v2, v3
	v_cvt_pk_bf16_f32 v150, v4, v5
	v_cvt_pk_bf16_f32 v151, v6, v7
	v_cvt_pk_f32_fp8_e32 v[0:1], v180
	v_cvt_pk_f32_fp8_sdwa v[2:3], v180 src0_sel:WORD_1
	v_cvt_pk_f32_fp8_e32 v[4:5], v181
	v_cvt_pk_f32_fp8_sdwa v[6:7], v181 src0_sel:WORD_1
	v_cvt_pk_bf16_f32 v152, v0, v1
	v_cvt_pk_bf16_f32 v153, v2, v3
	v_cvt_pk_bf16_f32 v154, v4, v5
	v_cvt_pk_bf16_f32 v155, v6, v7
	v_cvt_pk_f32_fp8_e32 v[0:1], v182
	v_cvt_pk_f32_fp8_sdwa v[2:3], v182 src0_sel:WORD_1
	v_cvt_pk_f32_fp8_e32 v[4:5], v183
	v_cvt_pk_f32_fp8_sdwa v[6:7], v183 src0_sel:WORD_1
	v_cvt_pk_bf16_f32 v156, v0, v1
	v_cvt_pk_bf16_f32 v157, v2, v3
	v_cvt_pk_bf16_f32 v158, v4, v5
	v_cvt_pk_bf16_f32 v159, v6, v7
	v_cvt_pk_f32_fp8_e32 v[0:1], v184
	v_cvt_pk_f32_fp8_sdwa v[2:3], v184 src0_sel:WORD_1
	v_cvt_pk_f32_fp8_e32 v[4:5], v185
	v_cvt_pk_f32_fp8_sdwa v[6:7], v185 src0_sel:WORD_1
	v_cvt_pk_bf16_f32 v160, v0, v1
	v_cvt_pk_bf16_f32 v161, v2, v3
	v_cvt_pk_bf16_f32 v162, v4, v5
	v_cvt_pk_bf16_f32 v163, v6, v7
	v_cvt_pk_f32_fp8_e32 v[0:1], v188
	v_cvt_pk_f32_fp8_sdwa v[2:3], v188 src0_sel:WORD_1
	v_cvt_pk_f32_fp8_e32 v[4:5], v189
	v_cvt_pk_f32_fp8_sdwa v[6:7], v189 src0_sel:WORD_1
	v_cvt_pk_bf16_f32 v164, v0, v1
	v_cvt_pk_bf16_f32 v165, v2, v3
	v_cvt_pk_bf16_f32 v166, v4, v5
	v_cvt_pk_bf16_f32 v167, v6, v7
	v_cvt_pk_f32_fp8_e32 v[0:1], v190
	v_cvt_pk_f32_fp8_sdwa v[2:3], v190 src0_sel:WORD_1
	v_cvt_pk_f32_fp8_e32 v[4:5], v191
	v_cvt_pk_f32_fp8_sdwa v[6:7], v191 src0_sel:WORD_1
	v_cvt_pk_bf16_f32 v168, v0, v1
	v_cvt_pk_bf16_f32 v169, v2, v3
	v_cvt_pk_bf16_f32 v170, v4, v5
	v_cvt_pk_bf16_f32 v171, v6, v7
	v_cvt_pk_f32_fp8_e32 v[0:1], v192
	v_cvt_pk_f32_fp8_sdwa v[2:3], v192 src0_sel:WORD_1
	v_cvt_pk_f32_fp8_e32 v[4:5], v193
	v_cvt_pk_f32_fp8_sdwa v[6:7], v193 src0_sel:WORD_1
	v_cvt_pk_bf16_f32 v172, v0, v1
	v_cvt_pk_bf16_f32 v173, v2, v3
	v_cvt_pk_bf16_f32 v174, v4, v5
	v_cvt_pk_bf16_f32 v175, v6, v7
	s_mov_b32 s101, 3

; __device__ __forceinline__ unsigned cvt_pk_bf16(float lo, float hi) { unsigned r; asm volatile("v_cvt_pk_bf16_f32 %0, %1, %2" : "=v"(r) : "v"(lo), "v"(hi)); return r; }
; #define DS_LOADQ(pa) do { const unsigned _q = roff(64 * (c.a0 + (pa)) + 32 * par + r32) + (unsigned)hi * 8u; _Pragma("unroll") for (int d0 = 0; d0 < 8; ++d0) qraw[d0] = *(const u32x2*)(zb + (_q + d0 * 16u)); } while (0)
; #define DS_RESET() do { m_reg = -1e30f; l_reg = 0.f; _Pragma("unroll") for (int d = 0; d < 4; ++d) _Pragma("unroll") for (int r = 0; r < 16; ++r) o[d][r] = 0.f; } while (0)
; __device__ __forceinline__ bf16x8 f8tob(u32x2 v) {
;     typedef float f2_ __attribute__((ext_vector_type(2)));
;     const f2_ a = __builtin_amdgcn_cvt_pk_f32_fp8((int)v.x, false), b = __builtin_amdgcn_cvt_pk_f32_fp8((int)v.x, true), c = __builtin_amdgcn_cvt_pk_f32_fp8((int)v.y, false), d = __builtin_amdgcn_cvt_pk_f32_fp8((int)v.y, true);
;     u32x4 w; w.x = cvt_pk_bf16(a[0], a[1]); w.y = cvt_pk_bf16(b[0], b[1]); w.z = cvt_pk_bf16(c[0], c[1]); w.w = cvt_pk_bf16(d[0], d[1]);
;     return __builtin_bit_cast(bf16x8, w);
; }
; __device__ __forceinline__ void datt_stream(LAS unsigned char* lds, const DattRun& c, const float C, const int wv) {
;     ...
;     bf16x8 qr[8]; u32x2 qraw[8]; float m_reg = -1e30f, l_reg = 0.f; f32x16 o[4];
;     ...
;     DS_LOADQ(pa0); DS_RESET();
;     auto compute = [&](const int rel, const int b, const int pa) __attribute__((always_inline)) {
;         const int tr = edge ? 0 : (rel == 1 ? 1 : (par ? (rel == 0 ? 2 : 0) : (rel == 2 ? 3 : 0))); const bool do0 = tr != 2, do1 = tr != 3;
;         if (rel == 0) {
; #pragma unroll
;             for (int d0 = 0; d0 < 8; ++d0) qr[d0] = f8tob(qraw[d0]); }
.LBB0_523:
	s_waitcnt vmcnt(6)
	v_cvt_scalef32_pk_bf16_fp8 v66, v212, 1.0
	v_cvt_scalef32_pk_bf16_fp8 v67, v212, 1.0 op_sel:[1,0,0]
	v_cvt_scalef32_pk_bf16_fp8 v68, v213, 1.0
	v_cvt_scalef32_pk_bf16_fp8 v69, v213, 1.0 op_sel:[1,0,0]
	ds_write_b128 v225, v[66:69]
	v_cvt_scalef32_pk_bf16_fp8 v66, v210, 1.0
	v_cvt_scalef32_pk_bf16_fp8 v67, v210, 1.0 op_sel:[1,0,0]
	v_cvt_scalef32_pk_bf16_fp8 v68, v211, 1.0
	v_cvt_scalef32_pk_bf16_fp8 v69, v211, 1.0 op_sel:[1,0,0]
	s_add_i32 s6, s57, 4
	ds_write_b128 v226, v[66:69] offset:32768
	s_waitcnt vmcnt(5)
	s_min_i32 s6, s6, s81
	v_cvt_scalef32_pk_bf16_fp8 v66, v204, 1.0
	v_cvt_scalef32_pk_bf16_fp8 v67, v204, 1.0 op_sel:[1,0,0]
	v_cvt_scalef32_pk_bf16_fp8 v68, v205, 1.0
	v_cvt_scalef32_pk_bf16_fp8 v69, v205, 1.0 op_sel:[1,0,0]
	v_add_u32_e32 v64, s6, v224
	ds_write_b128 v227, v[66:69]
	s_waitcnt vmcnt(4)
	v_lshl_add_u32 v64, v64, 6, v197
	v_cvt_scalef32_pk_bf16_fp8 v66, v200, 1.0
	v_cvt_scalef32_pk_bf16_fp8 v67, v200, 1.0 op_sel:[1,0,0]
	v_cvt_scalef32_pk_bf16_fp8 v68, v201, 1.0
	v_add_u32_e32 v70, 32, v64
	v_min_i32_e32 v70, s95, v70
	v_cmp_lt_i32_e32 vcc, s43, v64
	v_cvt_scalef32_pk_bf16_fp8 v69, v201, 1.0 op_sel:[1,0,0]
	v_min_i32_e32 v72, s95, v64
	s_nop 0
	v_cndmask_b32_e32 v70, 0, v70, vcc
	v_cmp_lt_i32_e32 vcc, -1, v64
	v_lshlrev_b32_e32 v70, s45, v70
	v_add_u32_e32 v70, s56, v70
	v_cndmask_b32_e32 v64, 0, v72, vcc
	v_lshlrev_b32_e32 v64, s45, v64
	v_mad_u64_u32 v[70:71], s[6:7], v70, s42, v[196:197]
	v_add_u32_e32 v64, s56, v64
	v_add_u32_e32 v71, 0x400, v70
	v_mad_u64_u32 v[72:73], s[6:7], v64, s42, v[196:197]
	v_add_u32_e32 v64, 0x400, v72
	global_load_dwordx2 v[204:205], v71, s[92:93]
	global_load_dwordx2 v[212:213], v64, s[92:93]
	global_load_dwordx2 v[210:211], v72, s[92:93]
	global_load_dwordx2 v[200:201], v70, s[92:93]
	ds_write_b128 v228, v[66:69] offset:32768
	s_cmp_eq_u32 s101, 2
	s_cbranch_scc0 .Ldatt_qc1_skip
	v_cvt_pk_f32_fp8_e32 v[66:67], v176
	v_cvt_pk_f32_fp8_sdwa v[68:69], v176 src0_sel:WORD_1
	v_cvt_pk_f32_fp8_e32 v[70:71], v177
	v_cvt_pk_f32_fp8_sdwa v[72:73], v177 src0_sel:WORD_1
	v_cvt_pk_bf16_f32 v144, v66, v67
	v_cvt_pk_bf16_f32 v145, v68, v69
	v_cvt_pk_bf16_f32 v146, v70, v71
	v_cvt_pk_bf16_f32 v147, v72, v73
	v_cvt_pk_f32_fp8_e32 v[66:67], v178
	v_cvt_pk_f32_fp8_sdwa v[68:69], v178 src0_sel:WORD_1
	v_cvt_pk_f32_fp8_e32 v[70:71], v179
	v_cvt_pk_f32_fp8_sdwa v[72:73], v179 src0_sel:WORD_1
	v_cvt_pk_bf16_f32 v148, v66, v67
	v_cvt_pk_bf16_f32 v149, v68, v69
	v_cvt_pk_bf16_f32 v150, v70, v71
	v_cvt_pk_bf16_f32 v151, v72, v73
	v_cvt_pk_f32_fp8_e32 v[66:67], v180
	v_cvt_pk_f32_fp8_sdwa v[68:69], v180 src0_sel:WORD_1
	v_cvt_pk_f32_fp8_e32 v[70:71], v181
	v_cvt_pk_f32_fp8_sdwa v[72:73], v181 src0_sel:WORD_1
	v_cvt_pk_bf16_f32 v152, v66, v67
	v_cvt_pk_bf16_f32 v153, v68, v69
	v_cvt_pk_bf16_f32 v154, v70, v71
	v_cvt_pk_bf16_f32 v155, v72, v73
	v_cvt_pk_f32_fp8_e32 v[66:67], v182
	v_cvt_pk_f32_fp8_sdwa v[68:69], v182 src0_sel:WORD_1
	v_cvt_pk_f32_fp8_e32 v[70:71], v183
	v_cvt_pk_f32_fp8_sdwa v[72:73], v183 src0_sel:WORD_1
	v_cvt_pk_bf16_f32 v156, v66, v67
	v_cvt_pk_bf16_f32 v157, v68, v69
	v_cvt_pk_bf16_f32 v158, v70, v71
	v_cvt_pk_bf16_f32 v159, v72, v73
	v_cvt_pk_f32_fp8_e32 v[66:67], v184
	v_cvt_pk_f32_fp8_sdwa v[68:69], v184 src0_sel:WORD_1
	v_cvt_pk_f32_fp8_e32 v[70:71], v185
	v_cvt_pk_f32_fp8_sdwa v[72:73], v185 src0_sel:WORD_1
	v_cvt_pk_bf16_f32 v160, v66, v67
	v_cvt_pk_bf16_f32 v161, v68, v69
	v_cvt_pk_bf16_f32 v162, v70, v71
	v_cvt_pk_bf16_f32 v163, v72, v73
	v_cvt_pk_f32_fp8_e32 v[66:67], v188
	v_cvt_pk_f32_fp8_sdwa v[68:69], v188 src0_sel:WORD_1
	v_cvt_pk_f32_fp8_e32 v[70:71], v189
	v_cvt_pk_f32_fp8_sdwa v[72:73], v189 src0_sel:WORD_1
	v_cvt_pk_bf16_f32 v164, v66, v67
	v_cvt_pk_bf16_f32 v165, v68, v69
	v_cvt_pk_bf16_f32 v166, v70, v71
	v_cvt_pk_bf16_f32 v167, v72, v73
	v_cvt_pk_f32_fp8_e32 v[66:67], v190
	v_cvt_pk_f32_fp8_sdwa v[68:69], v190 src0_sel:WORD_1
	v_cvt_pk_f32_fp8_e32 v[70:71], v191
	v_cvt_pk_f32_fp8_sdwa v[72:73], v191 src0_sel:WORD_1
	v_cvt_pk_bf16_f32 v168, v66, v67
	v_cvt_pk_bf16_f32 v169, v68, v69
	v_cvt_pk_bf16_f32 v170, v70, v71
	v_cvt_pk_bf16_f32 v171, v72, v73
	v_cvt_pk_f32_fp8_e32 v[66:67], v192
	v_cvt_pk_f32_fp8_sdwa v[68:69], v192 src0_sel:WORD_1
	v_cvt_pk_f32_fp8_e32 v[70:71], v193
	v_cvt_pk_f32_fp8_sdwa v[72:73], v193 src0_sel:WORD_1
	v_cvt_pk_bf16_f32 v172, v66, v67
	v_cvt_pk_bf16_f32 v173, v68, v69
	v_cvt_pk_bf16_f32 v174, v70, v71
	v_cvt_pk_bf16_f32 v175, v72, v73
	s_mov_b32 s101, 3
